# grid barrier: arrival atomic first, invalidate behind it, wait only for the atomic
# speedup vs baseline: 1.0114x; 1.0045x over previous
.LBB0_139:
	v_readlane_b32 s6, v255, 4
	v_readlane_b32 s7, v255, 5
	s_lshl_b64 s[6:7], s[6:7], 2
	v_readlane_b32 s3, v255, 2
	s_add_u32 s8, s3, s6
	v_readlane_b32 s3, v255, 3
	s_addc_u32 s9, s3, s7
	v_readlane_b32 s3, v255, 6
	s_lshl_b32 s3, s3, 8
	s_add_u32 s6, s8, s3
	s_addc_u32 s7, s9, 0
	v_mov_b32_e32 v2, 0x1000
	v_mov_b32_e32 v4, 1
	global_atomic_add v4, v2, v4, s[6:7] offset:1024 sc0
	buffer_inv sc1
	v_cvt_f32_u32_e32 v2, v3
	v_sub_u32_e32 v5, 0, v3
	v_rcp_iflag_f32_e32 v2, v2
	s_nop 0
	v_mul_f32_e32 v2, 0x4f7ffffe, v2
	v_cvt_u32_f32_e32 v2, v2
	v_mul_lo_u32 v5, v5, v2
	v_mul_hi_u32 v5, v2, v5
	v_add_u32_e32 v2, v2, v5
	s_waitcnt vmcnt(1)
	v_mul_hi_u32 v2, v4, v2
	v_mul_lo_u32 v5, v2, v3
	v_sub_u32_e32 v5, v4, v5
	v_add_u32_e32 v6, 1, v2
	v_cmp_ge_u32_e32 vcc, v5, v3
	v_add_u32_e32 v4, 1, v4
	s_nop 0
	v_cndmask_b32_e32 v2, v2, v6, vcc
	v_sub_u32_e32 v6, v5, v3
	v_cndmask_b32_e32 v5, v5, v6, vcc
	v_add_u32_e32 v6, 1, v2
	v_cmp_ge_u32_e32 vcc, v5, v3
	s_nop 1
	v_cndmask_b32_e32 v2, v2, v6, vcc
	v_mul_lo_u32 v5, v3, v2
	v_add_u32_e32 v3, v5, v3
	v_cmp_ne_u32_e32 vcc, v4, v3
	s_and_saveexec_b64 s[12:13], vcc
	s_xor_b64 s[12:13], exec, s[12:13]
	s_cbranch_execz .LBB0_153
	s_waitcnt lgkmcnt(0)
	v_mov_b32_e32 v1, 0x2000
	global_load_dword v1, v1, s[6:7] offset:1024 sc1
	s_add_u32 s16, s6, 0x2400
	s_addc_u32 s17, s7, 0
	s_waitcnt vmcnt(0)
	v_cmp_eq_u32_e32 vcc, v1, v2
	s_and_saveexec_b64 s[14:15], vcc
	s_cbranch_execz .LBB0_152
	s_mov_b32 s3, 1
	s_mov_b64 s[18:19], 0
	v_mov_b32_e32 v1, 0
	s_branch .LBB0_143

.LBB0_193:
	v_readlane_b32 s6, v255, 4
	v_readlane_b32 s7, v255, 5
	s_lshl_b64 s[6:7], s[6:7], 2
	v_readlane_b32 s3, v255, 2
	s_add_u32 s8, s3, s6
	v_readlane_b32 s3, v255, 3
	s_addc_u32 s9, s3, s7
	v_readlane_b32 s3, v255, 6
	s_lshl_b32 s3, s3, 8
	s_add_u32 s6, s8, s3
	s_addc_u32 s7, s9, 0
	v_mov_b32_e32 v2, 0x1000
	v_mov_b32_e32 v4, 1
	global_atomic_add v4, v2, v4, s[6:7] offset:1024 sc0
	buffer_inv sc1
	v_cvt_f32_u32_e32 v2, v3
	v_sub_u32_e32 v5, 0, v3
	v_rcp_iflag_f32_e32 v2, v2
	s_nop 0
	v_mul_f32_e32 v2, 0x4f7ffffe, v2
	v_cvt_u32_f32_e32 v2, v2
	v_mul_lo_u32 v5, v5, v2
	v_mul_hi_u32 v5, v2, v5
	v_add_u32_e32 v2, v2, v5
	s_waitcnt vmcnt(1)
	v_mul_hi_u32 v2, v4, v2
	v_mul_lo_u32 v5, v2, v3
	v_sub_u32_e32 v5, v4, v5
	v_add_u32_e32 v6, 1, v2
	v_cmp_ge_u32_e32 vcc, v5, v3
	v_add_u32_e32 v4, 1, v4
	s_nop 0
	v_cndmask_b32_e32 v2, v2, v6, vcc
	v_sub_u32_e32 v6, v5, v3
	v_cndmask_b32_e32 v5, v5, v6, vcc
	v_add_u32_e32 v6, 1, v2
	v_cmp_ge_u32_e32 vcc, v5, v3
	s_nop 1
	v_cndmask_b32_e32 v2, v2, v6, vcc
	v_mul_lo_u32 v5, v3, v2
	v_add_u32_e32 v3, v5, v3
	v_cmp_ne_u32_e32 vcc, v4, v3
	s_and_saveexec_b64 s[10:11], vcc
	s_xor_b64 s[10:11], exec, s[10:11]
	s_cbranch_execz .LBB0_207
	s_waitcnt lgkmcnt(0)
	v_mov_b32_e32 v1, 0x2000
	global_load_dword v1, v1, s[6:7] offset:1024 sc1
	s_add_u32 s14, s6, 0x2400
	s_addc_u32 s15, s7, 0
	s_waitcnt vmcnt(0)
	v_cmp_eq_u32_e32 vcc, v1, v2
	s_and_saveexec_b64 s[12:13], vcc
	s_cbranch_execz .LBB0_206
	s_mov_b32 s3, 1
	s_mov_b64 s[16:17], 0
	v_mov_b32_e32 v1, 0
	s_branch .LBB0_197

.LBB0_3030:
	v_readlane_b32 s4, v255, 4
	v_readlane_b32 s5, v255, 5
	s_lshl_b64 s[4:5], s[4:5], 2
	v_readlane_b32 s6, v255, 2
	s_add_u32 s6, s6, s4
	v_readlane_b32 s4, v255, 3
	s_addc_u32 s7, s4, s5
	v_readlane_b32 s4, v255, 6
	s_lshl_b32 s4, s4, 8
	s_add_u32 s4, s6, s4
	s_addc_u32 s5, s7, 0
	v_mov_b32_e32 v1, 0x1000
	v_mov_b32_e32 v3, 1
	global_atomic_add v3, v1, v3, s[4:5] offset:1024 sc0
	buffer_inv sc1
	v_cvt_f32_u32_e32 v1, v2
	v_sub_u32_e32 v4, 0, v2
	v_rcp_iflag_f32_e32 v1, v1
	s_nop 0
	v_mul_f32_e32 v1, 0x4f7ffffe, v1
	v_cvt_u32_f32_e32 v1, v1
	v_mul_lo_u32 v4, v4, v1
	v_mul_hi_u32 v4, v1, v4
	v_add_u32_e32 v1, v1, v4
	s_waitcnt vmcnt(1)
	v_mul_hi_u32 v1, v3, v1
	v_mul_lo_u32 v4, v1, v2
	v_sub_u32_e32 v4, v3, v4
	v_add_u32_e32 v5, 1, v1
	v_cmp_ge_u32_e32 vcc, v4, v2
	v_add_u32_e32 v3, 1, v3
	s_nop 0
	v_cndmask_b32_e32 v1, v1, v5, vcc
	v_sub_u32_e32 v5, v4, v2
	v_cndmask_b32_e32 v4, v4, v5, vcc
	v_add_u32_e32 v5, 1, v1
	v_cmp_ge_u32_e32 vcc, v4, v2
	s_nop 1
	v_cndmask_b32_e32 v1, v1, v5, vcc
	v_mul_lo_u32 v4, v2, v1
	v_add_u32_e32 v2, v4, v2
	v_cmp_ne_u32_e32 vcc, v3, v2
	s_and_saveexec_b64 s[8:9], vcc
	s_xor_b64 s[8:9], exec, s[8:9]
	s_cbranch_execz .LBB0_3044
	s_waitcnt lgkmcnt(0)
	v_mov_b32_e32 v0, 0x2000
	global_load_dword v0, v0, s[4:5] offset:1024 sc1
	s_add_u32 s12, s4, 0x2400
	s_addc_u32 s13, s5, 0
	s_waitcnt vmcnt(0)
	v_cmp_eq_u32_e32 vcc, v0, v1
	s_and_saveexec_b64 s[10:11], vcc
	s_cbranch_execz .LBB0_3043
	s_mov_b32 s28, 1
	s_mov_b64 s[14:15], 0
	v_mov_b32_e32 v0, 0
	s_branch .LBB0_3034
